# rmsnorm1 rows re-dealt inside each workgroup: none for the two waves that also build the S5 taps, 4 for the wave that builds the router bias, 12 for the other five
# speedup vs baseline: 1.0025x; 1.0025x over previous
; __device__ __forceinline__ void ph1_norm(const Args& a, int wave, int lane, int G, int bid) {
;     ...
;     {
;         const float* X = a.in[I_X]; const float* g1 = a.in[I_N1G]; bf16* HN = (bf16*)(a.ws + WS_HN); unsigned char* HN8 = (unsigned char*)(a.ws + WS_HN8);
;         const int RPW = (T + NGW - 1) / NGW, r0 = gw * RPW, r1 = min(T, r0 + RPW);
;         f32x4 vn[8], pa[8], pb[8]; int curb = -1;
;         if (r0 < r1) { const f32x4* xr = (const f32x4*)(X + (size_t)r0 * DM) + 2 * lane;
; #pragma unroll
;             for (int j = 0; j < 4; ++j) { vn[2 * j] = __builtin_nontemporal_load(xr + 128 * j); vn[2 * j + 1] = __builtin_nontemporal_load(xr + 128 * j + 1); } }
.LBB0_204:
	s_abs_i32 s33, s81
	s_waitcnt vmcnt(1)
	v_cvt_f32_u32_e32 v2, s33
	s_sub_i32 s46, 0, s33
	s_abs_i32 s45, s83
	s_xor_b32 s44, s83, s81
	v_rcp_iflag_f32_e32 v2, v2
	s_ashr_i32 s44, s44, 31
	v_mul_f32_e32 v2, 0x4f7ffffe, v2
	v_cvt_u32_f32_e32 v2, v2
	s_nop 0
	v_readfirstlane_b32 s47, v2
	s_mul_i32 s46, s46, s47
	s_mul_hi_u32 s46, s47, s46
	s_add_i32 s47, s47, s46
	s_mul_hi_u32 s46, s45, s47
	s_mul_i32 s47, s46, s33
	s_sub_i32 s45, s45, s47
	s_add_i32 s48, s46, 1
	s_sub_i32 s47, s45, s33
	s_cmp_ge_u32 s45, s33
	s_cselect_b32 s46, s48, s46
	s_cselect_b32 s45, s47, s45
	s_add_i32 s47, s46, 1
	s_cmp_ge_u32 s45, s33
	s_cselect_b32 s33, s47, s46
	s_xor_b32 s33, s33, s44
	s_sub_i32 s33, s33, s44
	s_mul_i32 s44, s33, s82
	s_add_i32 s33, s44, s33
	s_min_i32 s33, s33, 0x4000
	s_and_b32 s46, s82, 7
	s_andn2_b32 s47, s82, 7
	s_lshl_b32 s47, s47, 3
	s_sub_i32 s48, s46, 3
	s_mul_i32 s44, s48, 12
	s_add_i32 s44, s44, 4
	s_mov_b32 s33, 12
	s_cmp_lt_u32 s46, 3
	s_cselect_b32 s44, 0, s44
	s_cselect_b32 s33, 4, s33
	s_cmp_lt_u32 s46, 2
	s_cselect_b32 s33, 0, s33
	s_add_i32 s44, s44, s47
	s_add_i32 s33, s44, s33
	s_cmp_ge_i32 s44, s33
	s_cbranch_scc1 .LBB0_211
	s_ashr_i32 s45, s44, 31
	s_lshl_b64 s[70:71], s[44:45], 13
	v_lshl_add_u64 v[2:3], v[148:149], 0, s[70:71]
	s_movk_i32 s53, 0x1000
	s_mov_b64 s[46:47], 0x1000
	s_waitcnt lgkmcnt(0)
	v_add_co_u32_e32 v6, vcc, s53, v2
	s_mov_b64 s[48:49], 0x1800
	global_load_dwordx4 v[26:29], v[2:3], off offset:16 nt
	global_load_dwordx4 v[30:33], v[2:3], off nt
	global_load_dwordx4 v[18:21], v[2:3], off offset:2064 nt
	global_load_dwordx4 v[22:25], v[2:3], off offset:2048 nt
	v_lshl_add_u64 v[4:5], v[2:3], 0, s[46:47]
	v_addc_co_u32_e32 v7, vcc, 0, v3, vcc
	v_lshl_add_u64 v[2:3], v[2:3], 0, s[48:49]
	global_load_dwordx4 v[14:17], v[6:7], off nt
	global_load_dwordx4 v[10:13], v[4:5], off offset:16 nt
	s_nop 0
	global_load_dwordx4 v[6:9], v[6:7], off offset:2048 nt
	s_nop 0
	global_load_dwordx4 v[2:5], v[2:3], off offset:16 nt
	v_mbcnt_lo_u32_b32 v34, -1, 0
	v_mbcnt_hi_u32_b32 v34, -1, v34
	v_and_b32_e32 v35, 64, v34
	v_add_u32_e32 v35, 64, v35
	v_xor_b32_e32 v36, 1, v34
	v_cmp_lt_i32_e32 vcc, v36, v35
	s_lshl_b64 s[72:73], s[44:45], 12
	v_lshl_or_b32 v150, v178, 4, s72
	v_cndmask_b32_e32 v36, v34, v36, vcc
	v_lshlrev_b32_e32 v214, 2, v36
	v_xor_b32_e32 v36, 2, v34
	v_cmp_lt_i32_e32 vcc, v36, v35
	v_mov_b32_e32 v151, s73
	s_lshl_b64 s[72:73], s[44:45], 11
	v_cndmask_b32_e32 v36, v34, v36, vcc
	v_lshlrev_b32_e32 v215, 2, v36
	v_xor_b32_e32 v36, 4, v34
	v_cmp_lt_i32_e32 vcc, v36, v35
	v_readlane_b32 s0, v250, 17
	v_mov_b32_e32 v155, 0
	v_cndmask_b32_e32 v36, v34, v36, vcc
	v_lshlrev_b32_e32 v216, 2, v36
	v_xor_b32_e32 v36, 8, v34
	v_cmp_lt_i32_e32 vcc, v36, v35
	v_readlane_b32 s1, v250, 18
	s_add_u32 s70, s0, s70
	v_cndmask_b32_e32 v36, v34, v36, vcc
	v_lshlrev_b32_e32 v217, 2, v36
	v_xor_b32_e32 v36, 16, v34
	v_cmp_lt_i32_e32 vcc, v36, v35
	v_mov_b32_e32 v131, v155
	s_addc_u32 s71, s1, s71
	v_cndmask_b32_e32 v36, v34, v36, vcc
	v_lshlrev_b32_e32 v218, 2, v36
	v_xor_b32_e32 v36, 32, v34
	v_cmp_lt_i32_e32 vcc, v36, v35
	s_mov_b32 s84, -1
	v_lshl_or_b32 v152, v178, 3, s72
	v_cndmask_b32_e32 v34, v34, v36, vcc
	v_lshlrev_b32_e32 v219, 2, v34
	v_lshl_add_u64 v[34:35], s[70:71], 0, v[130:131]
	s_mov_b64 s[70:71], 0x2000
	v_mov_b32_e32 v153, s73
	v_lshl_add_u64 v[156:157], v[34:35], 0, s[70:71]
	v_mov_b32_e32 v131, 0x358637bd
	v_mov_b32_e32 v220, 0x260
	s_mov_b32 s74, 0xc3e00000
	v_mov_b32_e32 v221, 0x43e00000
	v_readlane_b32 s2, v250, 19
	v_readlane_b32 s3, v250, 20
	v_readlane_b32 s4, v250, 21
	v_readlane_b32 s5, v250, 22
	v_readlane_b32 s6, v250, 23
	v_readlane_b32 s7, v250, 24
	v_readlane_b32 s8, v250, 25
	v_readlane_b32 s9, v250, 26
	v_readlane_b32 s10, v250, 27
	v_readlane_b32 s11, v250, 28
	v_readlane_b32 s12, v250, 29
	v_readlane_b32 s13, v250, 30
	v_readlane_b32 s14, v250, 31
	v_readlane_b32 s15, v250, 32
	s_waitcnt vmcnt(7)
	v_mov_b64_e32 v[72:73], v[28:29]
	s_waitcnt vmcnt(6)
	v_mov_b64_e32 v[68:69], v[32:33]
	s_waitcnt vmcnt(5)
	v_mov_b64_e32 v[80:81], v[20:21]
	s_waitcnt vmcnt(4)
	v_mov_b64_e32 v[76:77], v[24:25]
	v_mov_b64_e32 v[66:67], v[30:31]
	v_mov_b64_e32 v[70:71], v[26:27]
	v_mov_b64_e32 v[74:75], v[22:23]
	s_waitcnt vmcnt(3)
	v_mov_b64_e32 v[84:85], v[16:17]
	s_waitcnt vmcnt(2)
	v_mov_b64_e32 v[88:89], v[12:13]
	s_waitcnt vmcnt(1)
	v_mov_b64_e32 v[92:93], v[8:9]
	s_waitcnt vmcnt(0)
	v_mov_b64_e32 v[96:97], v[4:5]
	v_mov_b64_e32 v[78:79], v[18:19]
	v_mov_b64_e32 v[82:83], v[14:15]
	v_mov_b64_e32 v[86:87], v[10:11]
	v_mov_b64_e32 v[90:91], v[6:7]
	v_mov_b64_e32 v[94:95], v[2:3]
	s_branch .LBB0_207

; __device__ __forceinline__ void ph1_norm(const Args& a, int wave, int lane, int G, int bid) {
;     ...
;     {
;         const float* X = a.in[I_X]; const float* g1 = a.in[I_N1G]; bf16* HN = (bf16*)(a.ws + WS_HN); unsigned char* HN8 = (unsigned char*)(a.ws + WS_HN8);
;         const int RPW = (T + NGW - 1) / NGW, r0 = gw * RPW, r1 = min(T, r0 + RPW);
;         f32x4 vn[8], pa[8], pb[8]; int curb = -1;
;         if (r0 < r1) { const f32x4* xr = (const f32x4*)(X + (size_t)r0 * DM) + 2 * lane;
; #pragma unroll
;             for (int j = 0; j < 4; ++j) { vn[2 * j] = __builtin_nontemporal_load(xr + 128 * j); vn[2 * j + 1] = __builtin_nontemporal_load(xr + 128 * j + 1); } }
.LBB0_212:
	s_and_b64 vcc, exec, s[44:45]
	s_mov_b64 s[16:17], s[38:39]
	s_cbranch_vccz .LBB0_337
	s_abs_i32 s33, s81
	v_cvt_f32_u32_e32 v2, s33
	s_sub_i32 s46, 0, s33
	s_abs_i32 s45, s83
	s_xor_b32 s44, s83, s81
	v_rcp_iflag_f32_e32 v2, v2
	s_ashr_i32 s44, s44, 31
	v_mul_f32_e32 v2, 0x4f7ffffe, v2
	v_cvt_u32_f32_e32 v2, v2
	s_nop 0
	v_readfirstlane_b32 s47, v2
	s_mul_i32 s46, s46, s47
	s_mul_hi_u32 s46, s47, s46
	s_add_i32 s47, s47, s46
	s_mul_hi_u32 s46, s45, s47
	s_mul_i32 s47, s46, s33
	s_sub_i32 s45, s45, s47
	s_add_i32 s48, s46, 1
	s_sub_i32 s47, s45, s33
	s_cmp_ge_u32 s45, s33
	s_cselect_b32 s46, s48, s46
	s_cselect_b32 s45, s47, s45
	s_add_i32 s47, s46, 1
	s_cmp_ge_u32 s45, s33
	s_cselect_b32 s33, s47, s46
	s_xor_b32 s33, s33, s44
	s_sub_i32 s33, s33, s44
	s_mul_i32 s44, s33, s82
	s_add_i32 s33, s44, s33
	s_min_i32 s33, s33, 0x4000
	s_and_b32 s46, s82, 7
	s_andn2_b32 s47, s82, 7
	s_lshl_b32 s47, s47, 3
	s_sub_i32 s48, s46, 3
	s_mul_i32 s44, s48, 12
	s_add_i32 s44, s44, 4
	s_mov_b32 s33, 12
	s_cmp_lt_u32 s46, 3
	s_cselect_b32 s44, 0, s44
	s_cselect_b32 s33, 4, s33
	s_cmp_lt_u32 s46, 2
	s_cselect_b32 s33, 0, s33
	s_add_i32 s44, s44, s47
	s_add_i32 s33, s44, s33
	s_cmp_ge_i32 s44, s33
	s_cbranch_scc1 .LBB0_220
	s_ashr_i32 s45, s44, 31
	s_lshl_b64 s[70:71], s[44:45], 13
	v_lshl_add_u64 v[2:3], v[148:149], 0, s[70:71]
	s_movk_i32 s53, 0x1000
	s_mov_b64 s[46:47], 0x1000
	s_waitcnt lgkmcnt(0)
	v_add_co_u32_e32 v6, vcc, s53, v2
	s_mov_b64 s[48:49], 0x1800
	global_load_dwordx4 v[26:29], v[2:3], off offset:16 nt
	global_load_dwordx4 v[30:33], v[2:3], off nt
	global_load_dwordx4 v[18:21], v[2:3], off offset:2064 nt
	global_load_dwordx4 v[22:25], v[2:3], off offset:2048 nt
	v_lshl_add_u64 v[4:5], v[2:3], 0, s[46:47]
	v_addc_co_u32_e32 v7, vcc, 0, v3, vcc
	v_lshl_add_u64 v[2:3], v[2:3], 0, s[48:49]
	global_load_dwordx4 v[14:17], v[6:7], off nt
	global_load_dwordx4 v[10:13], v[4:5], off offset:16 nt
	s_nop 0
	global_load_dwordx4 v[6:9], v[6:7], off offset:2048 nt
	s_nop 0
	global_load_dwordx4 v[2:5], v[2:3], off offset:16 nt
	v_mbcnt_lo_u32_b32 v34, -1, 0
	v_mbcnt_hi_u32_b32 v34, -1, v34
	v_and_b32_e32 v35, 64, v34
	v_add_u32_e32 v35, 64, v35
	v_xor_b32_e32 v36, 1, v34
	v_cmp_lt_i32_e32 vcc, v36, v35
	s_lshl_b64 s[72:73], s[44:45], 12
	v_lshl_or_b32 v148, v178, 4, s72
	v_cndmask_b32_e32 v36, v34, v36, vcc
	v_lshlrev_b32_e32 v156, 2, v36
	v_xor_b32_e32 v36, 2, v34
	v_cmp_lt_i32_e32 vcc, v36, v35
	v_mov_b32_e32 v149, s73
	s_lshl_b64 s[72:73], s[44:45], 11
	v_cndmask_b32_e32 v36, v34, v36, vcc
	v_lshlrev_b32_e32 v157, 2, v36
	v_xor_b32_e32 v36, 4, v34
	v_cmp_lt_i32_e32 vcc, v36, v35
	v_readlane_b32 s0, v250, 17
	v_mov_b32_e32 v153, 0
	v_cndmask_b32_e32 v36, v34, v36, vcc
	v_lshlrev_b32_e32 v214, 2, v36
	v_xor_b32_e32 v36, 8, v34
	v_cmp_lt_i32_e32 vcc, v36, v35
	v_readlane_b32 s1, v250, 18
	s_add_u32 s70, s0, s70
	v_cndmask_b32_e32 v36, v34, v36, vcc
	v_lshlrev_b32_e32 v215, 2, v36
	v_xor_b32_e32 v36, 16, v34
	v_cmp_lt_i32_e32 vcc, v36, v35
	v_mov_b32_e32 v131, v153
	s_addc_u32 s71, s1, s71
	v_cndmask_b32_e32 v36, v34, v36, vcc
	v_lshlrev_b32_e32 v216, 2, v36
	v_xor_b32_e32 v36, 32, v34
	v_cmp_lt_i32_e32 vcc, v36, v35
	s_mov_b32 s82, -1
	v_lshl_or_b32 v150, v178, 3, s72
	v_cndmask_b32_e32 v34, v34, v36, vcc
	v_lshlrev_b32_e32 v217, 2, v34
	v_lshl_add_u64 v[34:35], s[70:71], 0, v[130:131]
	s_mov_b64 s[70:71], 0x2000
	v_mov_b32_e32 v151, s73
	v_lshl_add_u64 v[154:155], v[34:35], 0, s[70:71]
	v_mov_b32_e32 v131, 0x358637bd
	v_mov_b32_e32 v218, 0x260
	s_mov_b32 s74, 0xc3e00000
	v_mov_b32_e32 v219, 0x43e00000
	v_readlane_b32 s2, v250, 19
	v_readlane_b32 s3, v250, 20
	v_readlane_b32 s4, v250, 21
	v_readlane_b32 s5, v250, 22
	v_readlane_b32 s6, v250, 23
	v_readlane_b32 s7, v250, 24
	v_readlane_b32 s8, v250, 25
	v_readlane_b32 s9, v250, 26
	v_readlane_b32 s10, v250, 27
	v_readlane_b32 s11, v250, 28
	v_readlane_b32 s12, v250, 29
	v_readlane_b32 s13, v250, 30
	v_readlane_b32 s14, v250, 31
	v_readlane_b32 s15, v250, 32
	s_waitcnt vmcnt(7)
	v_mov_b64_e32 v[72:73], v[28:29]
	s_waitcnt vmcnt(6)
	v_mov_b64_e32 v[68:69], v[32:33]
	s_waitcnt vmcnt(5)
	v_mov_b64_e32 v[80:81], v[20:21]
	s_waitcnt vmcnt(4)
	v_mov_b64_e32 v[76:77], v[24:25]
	v_mov_b64_e32 v[66:67], v[30:31]
	v_mov_b64_e32 v[70:71], v[26:27]
	v_mov_b64_e32 v[74:75], v[22:23]
	s_waitcnt vmcnt(3)
	v_mov_b64_e32 v[84:85], v[16:17]
	s_waitcnt vmcnt(2)
	v_mov_b64_e32 v[88:89], v[12:13]
	s_waitcnt vmcnt(1)
	v_mov_b64_e32 v[92:93], v[8:9]
	s_waitcnt vmcnt(0)
	v_mov_b64_e32 v[96:97], v[4:5]
	v_mov_b64_e32 v[78:79], v[18:19]
	v_mov_b64_e32 v[82:83], v[14:15]
	v_mov_b64_e32 v[86:87], v[10:11]
	v_mov_b64_e32 v[90:91], v[6:7]
	v_mov_b64_e32 v[94:95], v[2:3]
	s_branch .LBB0_216
